# P9 / P10 phase start: first-unit table lookups issued together with the tile-count load (one dependent round trip fewer per phase)
# baseline (speedup 1.0000x reference)
;     __device__ __forceinline__ bool next(int i, U& u) const {
;         const int nt = tile[3 * NTILE_MAX]; const int L = i * G + c; if (L >= nt * 4) return false;
;         const int t = L >> 2; u.pn = L & 3; const int e = tile[t]; u.row0 = tile[NTILE_MAX + t]; u.nrows = tile[2 * NTILE_MAX + t];
;         u.A = H2; u.B = W + ((size_t)e * 1024 + u.pn * 256) * 2048; return true;
.LBB0_1278:
	s_cmp_gt_i32 s94, 9
	s_cselect_b64 s[0:1], -1, 0
	s_cmp_lt_i32 s95, 10
	s_cselect_b64 s[2:3], -1, 0
	s_or_b64 s[0:1], s[0:1], s[2:3]
	s_and_b64 vcc, exec, s[0:1]
	s_waitcnt lgkmcnt(0)
	v_readlane_b32 s71, v246, 2
	v_readlane_b32 s72, v246, 22
	s_cbranch_vccnz .LBB0_1371
	v_mov_b32_e32 v1, v0
	s_movk_i32 s0, 0x400
	v_mov_b32_e32 v1, 0x39e72000
	global_load_dword v1, v1, s[92:93] offset:256
	s_add_u32 s10, s92, 0x1a200000
	s_addc_u32 s11, s93, 0
	s_add_u32 s33, s92, 0x9e00000
	s_addc_u32 s38, s93, 0
	s_add_u32 s39, s92, 0x39e70000
	s_addc_u32 s44, s93, 0
	s_add_u32 s12, s92, 0x39e72100
	s_addc_u32 s13, s93, 0
	v_readfirstlane_b32 s6, v0
	s_ashr_i32 s4, s71, 2
	s_ashr_i32 s5, s4, 31
	s_and_b32 s65, s71, 3
	s_lshl_b64 s[4:5], s[4:5], 2
	s_add_u32 s4, s39, s4
	s_addc_u32 s5, s44, s5
	v_mov_b32_e32 v4, 0
	global_load_dword v2, v4, s[4:5]
	v_mov_b32_e32 v3, 0x1000
	global_load_dword v226, v4, s[4:5] offset:2816
	global_load_dword v227, v3, s[4:5] offset:1536
	s_waitcnt vmcnt(0)
	v_readfirstlane_b32 s1, v1
	s_mov_b32 s98, s1
	s_lshl_b32 s1, s1, 2
	s_cmp_lt_i32 s71, s1
	s_cselect_b64 s[2:3], -1, 0
	s_cmp_ge_i32 s71, s1
	s_cbranch_scc1 .LBB0_1281
	s_lshl_b32 s1, s65, 19
	s_mov_b64 s[34:35], s[10:11]
	s_waitcnt vmcnt(2)
	v_readfirstlane_b32 s4, v2
	s_ashr_i32 s5, s4, 31
	s_lshl_b64 s[4:5], s[4:5], 21
	s_add_u32 s4, s33, s4
	s_addc_u32 s5, s38, s5
	s_add_u32 s4, s4, s1
	s_addc_u32 s5, s5, 0
	s_andn2_b64 vcc, exec, s[2:3]
	s_cbranch_vccz .LBB0_1282
	s_branch .LBB0_1321

;     __device__ __forceinline__ bool next(int i, U& u) const {
;         const int nt = tile[3 * NTILE_MAX]; const int L = i * G + c; if (L >= nt * 8) return false;
;         const int t = L >> 3; u.pn = L & 7; const int e = tile[t]; u.row0 = tile[NTILE_MAX + t]; u.nrows = tile[2 * NTILE_MAX + t];
;         u.A = ACT + (size_t)u.row0 * 512; u.B = W + ((size_t)e * 2048 + u.pn * 256) * 512; return true;
.LBB0_1371:
	s_cmp_gt_i32 s94, 10
	s_cselect_b64 s[0:1], -1, 0
	s_cmp_lt_i32 s95, 11
	s_cselect_b64 s[2:3], -1, 0
	s_or_b64 s[0:1], s[0:1], s[2:3]
	s_and_b64 vcc, exec, s[0:1]
	s_cbranch_vccnz .LBB0_1462
	v_mov_b32_e32 v1, v0
	s_movk_i32 s0, 0x100
	v_mov_b32_e32 v1, 0x39e72000
	global_load_dword v1, v1, s[92:93] offset:256
	s_add_u32 s4, s92, 0x30b00000
	s_addc_u32 s5, s93, 0
	s_add_u32 s21, s92, 0x1c00000
	s_addc_u32 s28, s93, 0
	s_add_u32 s29, s92, 0x39e70000
	s_addc_u32 s30, s93, 0
	s_add_u32 s6, s92, 0x39e72100
	s_addc_u32 s7, s93, 0
	v_readfirstlane_b32 s16, v0
	s_ashr_i32 s2, s71, 3
	s_ashr_i32 s3, s2, 31
	s_and_b32 s54, s71, 7
	s_lshl_b64 s[2:3], s[2:3], 2
	s_add_u32 s2, s29, s2
	s_addc_u32 s3, s30, s3
	v_mov_b32_e32 v3, 0
	global_load_dword v2, v3, s[2:3]
	global_load_dword v198, v3, s[2:3] offset:2816
	v_mov_b32_e32 v4, 0x1000
	global_load_dword v5, v4, s[2:3] offset:1536
	s_waitcnt vmcnt(0)
	v_readfirstlane_b32 s1, v1
	s_mov_b32 s98, s1
	s_lshl_b32 s1, s1, 3
	s_cmp_lt_i32 s71, s1
	s_cselect_b64 s[8:9], -1, 0
	s_cmp_ge_i32 s71, s1
	s_cbranch_scc1 .LBB0_1374
	v_mov_b32_e32 v1, v5
	s_lshl_b32 s1, s54, 17
	v_readfirstlane_b32 s2, v2
	s_ashr_i32 s3, s2, 31
	s_lshl_b64 s[2:3], s[2:3], 20
	s_add_u32 s2, s21, s2
	v_ashrrev_i32_e32 v199, 31, v198
	s_addc_u32 s3, s28, s3
	v_lshlrev_b64 v[2:3], 9, v[198:199]
	s_add_u32 s2, s2, s1
	v_lshl_add_u64 v[220:221], s[4:5], 0, v[2:3]
	s_addc_u32 s3, s3, 0
	s_andn2_b64 vcc, exec, s[8:9]
	s_cbranch_vccz .LBB0_1375
	s_branch .LBB0_1412
